# combo12a + Gray-code MFMA order in the bf16 P6 score-GEMM loop (consecutive MFMAs share one fragment operand)
# speedup vs baseline: 1.0057x; 1.0057x over previous
.LBB0_687:
	s_add_u32 s72, s24, 0xfff00000
	s_addc_u32 s73, s25, -1
	s_mov_b32 m0, s44
	s_nop 0
	global_load_lds_dwordx4 v128, s[72:73]
	s_mov_b32 m0, s45
	s_nop 0
	global_load_lds_dwordx4 v130, s[72:73]
	ds_read_b128 v[160:163], v142
	ds_read_b128 v[164:167], v143
	ds_read_b128 v[168:171], v144
	ds_read_b128 v[172:175], v145
	ds_read_b128 v[176:179], v146
	ds_read_b128 v[180:183], v147
	ds_read_b128 v[184:187], v148
	ds_read_b128 v[188:191], v149
	s_add_u32 s26, s24, 0xfff00080
	s_addc_u32 s27, s25, -1
	s_cmp_eq_u32 s54, 60
	s_cselect_b32 s29, s19, s27
	s_cselect_b32 s28, s50, s26
	s_cselect_b32 s27, s17, s53
	s_cselect_b32 s26, s51, s52
	s_add_i32 m0, s33, 0xc000
	ds_read_b128 v[192:195], v158
	ds_read_b128 v[196:199], v158 offset:1024
	ds_read_b128 v[200:203], v158 offset:2048
	ds_read_b128 v[204:207], v158 offset:3072
	ds_read_b128 v[208:211], v158 offset:4096
	ds_read_b128 v[212:215], v158 offset:5120
	ds_read_b128 v[216:219], v158 offset:6144
	ds_read_b128 v[220:223], v158 offset:7168
	global_load_lds_dwordx4 v134, s[24:25]
	s_add_i32 m0, s33, 0xe000
	s_nop 0
	global_load_lds_dwordx4 v136, s[24:25]
	s_waitcnt vmcnt(8)
	s_waitcnt lgkmcnt(0)
	s_barrier
	s_setprio 1
	s_waitcnt lgkmcnt(0)
	v_mfma_f32_16x16x32_bf16 v[124:127], v[160:163], v[192:195], v[124:127]
	v_mfma_f32_16x16x32_bf16 v[120:123], v[168:171], v[192:195], v[120:123]
	v_mfma_f32_16x16x32_bf16 v[112:115], v[168:171], v[200:203], v[112:115]
	v_mfma_f32_16x16x32_bf16 v[116:119], v[160:163], v[200:203], v[116:119]
	v_mfma_f32_16x16x32_bf16 v[108:111], v[160:163], v[208:211], v[108:111]
	v_mfma_f32_16x16x32_bf16 v[104:107], v[168:171], v[208:211], v[104:107]
	v_mfma_f32_16x16x32_bf16 v[96:99], v[168:171], v[216:219], v[96:99]
	v_mfma_f32_16x16x32_bf16 v[100:103], v[160:163], v[216:219], v[100:103]
	v_mfma_f32_16x16x32_bf16 v[124:127], v[164:167], v[196:199], v[124:127]
	v_mfma_f32_16x16x32_bf16 v[120:123], v[172:175], v[196:199], v[120:123]
	v_mfma_f32_16x16x32_bf16 v[112:115], v[172:175], v[204:207], v[112:115]
	v_mfma_f32_16x16x32_bf16 v[116:119], v[164:167], v[204:207], v[116:119]
	v_mfma_f32_16x16x32_bf16 v[108:111], v[164:167], v[212:215], v[108:111]
	v_mfma_f32_16x16x32_bf16 v[104:107], v[172:175], v[212:215], v[104:107]
	v_mfma_f32_16x16x32_bf16 v[96:99], v[172:175], v[220:223], v[96:99]
	v_mfma_f32_16x16x32_bf16 v[100:103], v[164:167], v[220:223], v[100:103]
	s_setprio 0
	s_setprio 1
	v_mfma_f32_16x16x32_bf16 v[92:95], v[176:179], v[192:195], v[92:95]
	v_mfma_f32_16x16x32_bf16 v[88:91], v[184:187], v[192:195], v[88:91]
	v_mfma_f32_16x16x32_bf16 v[80:83], v[184:187], v[200:203], v[80:83]
	v_mfma_f32_16x16x32_bf16 v[84:87], v[176:179], v[200:203], v[84:87]
	v_mfma_f32_16x16x32_bf16 v[76:79], v[176:179], v[208:211], v[76:79]
	v_mfma_f32_16x16x32_bf16 v[72:75], v[184:187], v[208:211], v[72:75]
	v_mfma_f32_16x16x32_bf16 v[64:67], v[184:187], v[216:219], v[64:67]
	v_mfma_f32_16x16x32_bf16 v[68:71], v[176:179], v[216:219], v[68:71]
	v_mfma_f32_16x16x32_bf16 v[92:95], v[180:183], v[196:199], v[92:95]
	v_mfma_f32_16x16x32_bf16 v[88:91], v[188:191], v[196:199], v[88:91]
	v_mfma_f32_16x16x32_bf16 v[80:83], v[188:191], v[204:207], v[80:83]
	v_mfma_f32_16x16x32_bf16 v[84:87], v[180:183], v[204:207], v[84:87]
	v_mfma_f32_16x16x32_bf16 v[76:79], v[180:183], v[212:215], v[76:79]
	v_mfma_f32_16x16x32_bf16 v[72:75], v[188:191], v[212:215], v[72:75]
	v_mfma_f32_16x16x32_bf16 v[64:67], v[188:191], v[220:223], v[64:67]
	v_mfma_f32_16x16x32_bf16 v[68:71], v[180:183], v[220:223], v[68:71]
	s_setprio 0
	s_barrier
	s_mov_b32 m0, s34
	v_lshl_add_u64 v[224:225], s[26:27], 0, v[128:129]
	s_add_u32 s56, s26, 0x100000
	ds_read_b128 v[192:195], v158 offset:16384
	ds_read_b128 v[196:199], v158 offset:17408
	ds_read_b128 v[200:203], v158 offset:18432
	ds_read_b128 v[204:207], v158 offset:19456
	ds_read_b128 v[208:211], v158 offset:20480
	ds_read_b128 v[212:215], v158 offset:21504
	ds_read_b128 v[216:219], v158 offset:22528
	ds_read_b128 v[220:223], v158 offset:23552
	global_load_lds_dwordx4 v[224:225], off
	v_lshl_add_u64 v[226:227], s[26:27], 0, v[130:131]
	s_mov_b32 m0, s35
	s_addc_u32 s57, s27, 0
	global_load_lds_dwordx4 v[226:227], off
	s_mov_b32 m0, s36
	s_nop 0
	global_load_lds_dwordx4 v128, s[56:57]
	s_mov_b32 m0, s37
	s_nop 0
	global_load_lds_dwordx4 v130, s[56:57]
	s_waitcnt vmcnt(6)
	s_waitcnt lgkmcnt(0)
	s_barrier
	s_setprio 1
	s_waitcnt lgkmcnt(0)
	v_mfma_f32_16x16x32_bf16 v[60:63], v[160:163], v[192:195], v[60:63]
	v_mfma_f32_16x16x32_bf16 v[56:59], v[168:171], v[192:195], v[56:59]
	v_mfma_f32_16x16x32_bf16 v[48:51], v[168:171], v[200:203], v[48:51]
	v_mfma_f32_16x16x32_bf16 v[52:55], v[160:163], v[200:203], v[52:55]
	v_mfma_f32_16x16x32_bf16 v[44:47], v[160:163], v[208:211], v[44:47]
	v_mfma_f32_16x16x32_bf16 v[40:43], v[168:171], v[208:211], v[40:43]
	v_mfma_f32_16x16x32_bf16 v[32:35], v[168:171], v[216:219], v[32:35]
	v_mfma_f32_16x16x32_bf16 v[36:39], v[160:163], v[216:219], v[36:39]
	v_mfma_f32_16x16x32_bf16 v[60:63], v[164:167], v[196:199], v[60:63]
	v_mfma_f32_16x16x32_bf16 v[56:59], v[172:175], v[196:199], v[56:59]
	v_mfma_f32_16x16x32_bf16 v[48:51], v[172:175], v[204:207], v[48:51]
	v_mfma_f32_16x16x32_bf16 v[52:55], v[164:167], v[204:207], v[52:55]
	v_mfma_f32_16x16x32_bf16 v[44:47], v[164:167], v[212:215], v[44:47]
	v_mfma_f32_16x16x32_bf16 v[40:43], v[172:175], v[212:215], v[40:43]
	v_mfma_f32_16x16x32_bf16 v[32:35], v[172:175], v[220:223], v[32:35]
	v_mfma_f32_16x16x32_bf16 v[36:39], v[164:167], v[220:223], v[36:39]
	s_setprio 0
	s_setprio 1
	v_mfma_f32_16x16x32_bf16 v[28:31], v[176:179], v[192:195], v[28:31]
	v_mfma_f32_16x16x32_bf16 v[24:27], v[184:187], v[192:195], v[24:27]
	v_mfma_f32_16x16x32_bf16 v[16:19], v[184:187], v[200:203], v[16:19]
	v_mfma_f32_16x16x32_bf16 v[20:23], v[176:179], v[200:203], v[20:23]
	v_mfma_f32_16x16x32_bf16 v[12:15], v[176:179], v[208:211], v[12:15]
	v_mfma_f32_16x16x32_bf16 v[8:11], v[184:187], v[208:211], v[8:11]
	v_mfma_f32_16x16x32_bf16 v[0:3], v[184:187], v[216:219], v[0:3]
	v_mfma_f32_16x16x32_bf16 v[4:7], v[176:179], v[216:219], v[4:7]
	v_mfma_f32_16x16x32_bf16 v[28:31], v[180:183], v[196:199], v[28:31]
	v_mfma_f32_16x16x32_bf16 v[24:27], v[188:191], v[196:199], v[24:27]
	v_mfma_f32_16x16x32_bf16 v[16:19], v[188:191], v[204:207], v[16:19]
	v_mfma_f32_16x16x32_bf16 v[20:23], v[180:183], v[204:207], v[20:23]
	v_mfma_f32_16x16x32_bf16 v[12:15], v[180:183], v[212:215], v[12:15]
	v_mfma_f32_16x16x32_bf16 v[8:11], v[188:191], v[212:215], v[8:11]
	v_mfma_f32_16x16x32_bf16 v[0:3], v[188:191], v[220:223], v[0:3]
	v_mfma_f32_16x16x32_bf16 v[4:7], v[180:183], v[220:223], v[4:7]
	s_setprio 0
	s_barrier
	s_mov_b32 m0, s33
	s_nop 0
	global_load_lds_dwordx4 v128, s[28:29]
	s_mov_b32 m0, s38
	s_nop 0
	global_load_lds_dwordx4 v130, s[28:29]
	ds_read_b128 v[160:163], v150
	ds_read_b128 v[164:167], v151
	ds_read_b128 v[168:171], v152
	ds_read_b128 v[172:175], v153
	ds_read_b128 v[176:179], v154
	ds_read_b128 v[180:183], v155
	ds_read_b128 v[184:187], v156
	ds_read_b128 v[188:191], v157
	s_add_u32 s28, s28, 0x100000
	s_addc_u32 s29, s29, 0
	s_mov_b32 m0, s39
	ds_read_b128 v[192:195], v158 offset:32768
	ds_read_b128 v[196:199], v158 offset:33792
	ds_read_b128 v[200:203], v158 offset:34816
	ds_read_b128 v[204:207], v158 offset:35840
	ds_read_b128 v[208:211], v158 offset:36864
	ds_read_b128 v[212:215], v158 offset:37888
	ds_read_b128 v[216:219], v158 offset:38912
	ds_read_b128 v[220:223], v158 offset:39936
	global_load_lds_dwordx4 v128, s[28:29]
	s_mov_b32 m0, s40
	s_nop 0
	global_load_lds_dwordx4 v130, s[28:29]
	s_waitcnt vmcnt(8)
	s_waitcnt lgkmcnt(0)
	s_barrier
	s_setprio 1
	s_waitcnt lgkmcnt(0)
	v_mfma_f32_16x16x32_bf16 v[124:127], v[160:163], v[192:195], v[124:127]
	v_mfma_f32_16x16x32_bf16 v[120:123], v[168:171], v[192:195], v[120:123]
	v_mfma_f32_16x16x32_bf16 v[112:115], v[168:171], v[200:203], v[112:115]
	v_mfma_f32_16x16x32_bf16 v[116:119], v[160:163], v[200:203], v[116:119]
	v_mfma_f32_16x16x32_bf16 v[108:111], v[160:163], v[208:211], v[108:111]
	v_mfma_f32_16x16x32_bf16 v[104:107], v[168:171], v[208:211], v[104:107]
	v_mfma_f32_16x16x32_bf16 v[96:99], v[168:171], v[216:219], v[96:99]
	v_mfma_f32_16x16x32_bf16 v[100:103], v[160:163], v[216:219], v[100:103]
	v_mfma_f32_16x16x32_bf16 v[124:127], v[164:167], v[196:199], v[124:127]
	v_mfma_f32_16x16x32_bf16 v[120:123], v[172:175], v[196:199], v[120:123]
	v_mfma_f32_16x16x32_bf16 v[112:115], v[172:175], v[204:207], v[112:115]
	v_mfma_f32_16x16x32_bf16 v[116:119], v[164:167], v[204:207], v[116:119]
	v_mfma_f32_16x16x32_bf16 v[108:111], v[164:167], v[212:215], v[108:111]
	v_mfma_f32_16x16x32_bf16 v[104:107], v[172:175], v[212:215], v[104:107]
	v_mfma_f32_16x16x32_bf16 v[96:99], v[172:175], v[220:223], v[96:99]
	v_mfma_f32_16x16x32_bf16 v[100:103], v[164:167], v[220:223], v[100:103]
	s_setprio 0
	s_setprio 1
	v_mfma_f32_16x16x32_bf16 v[92:95], v[176:179], v[192:195], v[92:95]
	v_mfma_f32_16x16x32_bf16 v[88:91], v[184:187], v[192:195], v[88:91]
	v_mfma_f32_16x16x32_bf16 v[80:83], v[184:187], v[200:203], v[80:83]
	v_mfma_f32_16x16x32_bf16 v[84:87], v[176:179], v[200:203], v[84:87]
	v_mfma_f32_16x16x32_bf16 v[76:79], v[176:179], v[208:211], v[76:79]
	v_mfma_f32_16x16x32_bf16 v[72:75], v[184:187], v[208:211], v[72:75]
	v_mfma_f32_16x16x32_bf16 v[64:67], v[184:187], v[216:219], v[64:67]
	v_mfma_f32_16x16x32_bf16 v[68:71], v[176:179], v[216:219], v[68:71]
	v_mfma_f32_16x16x32_bf16 v[92:95], v[180:183], v[196:199], v[92:95]
	v_mfma_f32_16x16x32_bf16 v[88:91], v[188:191], v[196:199], v[88:91]
	v_mfma_f32_16x16x32_bf16 v[80:83], v[188:191], v[204:207], v[80:83]
	v_mfma_f32_16x16x32_bf16 v[84:87], v[180:183], v[204:207], v[84:87]
	v_mfma_f32_16x16x32_bf16 v[76:79], v[180:183], v[212:215], v[76:79]
	v_mfma_f32_16x16x32_bf16 v[72:75], v[188:191], v[212:215], v[72:75]
	v_mfma_f32_16x16x32_bf16 v[64:67], v[188:191], v[220:223], v[64:67]
	v_mfma_f32_16x16x32_bf16 v[68:71], v[180:183], v[220:223], v[68:71]
	s_setprio 0
	s_barrier
	s_mov_b32 m0, s42
	v_lshl_add_u64 v[224:225], v[224:225], 0, s[10:11]
	s_add_u32 s26, s26, 0x100080
	ds_read_b128 v[192:195], v158 offset:49152
	ds_read_b128 v[196:199], v158 offset:50176
	ds_read_b128 v[200:203], v158 offset:51200
	ds_read_b128 v[204:207], v158 offset:52224
	ds_read_b128 v[208:211], v158 offset:53248
	ds_read_b128 v[212:215], v158 offset:54272
	ds_read_b128 v[216:219], v158 offset:55296
	ds_read_b128 v[220:223], v158 offset:56320
	global_load_lds_dwordx4 v[224:225], off
	v_lshl_add_u64 v[224:225], v[226:227], 0, s[10:11]
	s_mov_b32 m0, s43
	s_addc_u32 s27, s27, 0
	global_load_lds_dwordx4 v[224:225], off
	s_mov_b32 m0, s46
	s_nop 0
	global_load_lds_dwordx4 v128, s[26:27]
	s_mov_b32 m0, s47
	s_nop 0
	global_load_lds_dwordx4 v130, s[26:27]
	s_waitcnt vmcnt(6)
	s_waitcnt lgkmcnt(0)
	s_barrier
	s_setprio 1
	s_waitcnt lgkmcnt(0)
	v_mfma_f32_16x16x32_bf16 v[60:63], v[160:163], v[192:195], v[60:63]
	v_mfma_f32_16x16x32_bf16 v[56:59], v[168:171], v[192:195], v[56:59]
	v_mfma_f32_16x16x32_bf16 v[48:51], v[168:171], v[200:203], v[48:51]
	v_mfma_f32_16x16x32_bf16 v[52:55], v[160:163], v[200:203], v[52:55]
	v_mfma_f32_16x16x32_bf16 v[44:47], v[160:163], v[208:211], v[44:47]
	v_mfma_f32_16x16x32_bf16 v[40:43], v[168:171], v[208:211], v[40:43]
	v_mfma_f32_16x16x32_bf16 v[32:35], v[168:171], v[216:219], v[32:35]
	v_mfma_f32_16x16x32_bf16 v[36:39], v[160:163], v[216:219], v[36:39]
	v_mfma_f32_16x16x32_bf16 v[60:63], v[164:167], v[196:199], v[60:63]
	v_mfma_f32_16x16x32_bf16 v[56:59], v[172:175], v[196:199], v[56:59]
	v_mfma_f32_16x16x32_bf16 v[48:51], v[172:175], v[204:207], v[48:51]
	v_mfma_f32_16x16x32_bf16 v[52:55], v[164:167], v[204:207], v[52:55]
	v_mfma_f32_16x16x32_bf16 v[44:47], v[164:167], v[212:215], v[44:47]
	v_mfma_f32_16x16x32_bf16 v[40:43], v[172:175], v[212:215], v[40:43]
	v_mfma_f32_16x16x32_bf16 v[32:35], v[172:175], v[220:223], v[32:35]
	v_mfma_f32_16x16x32_bf16 v[36:39], v[164:167], v[220:223], v[36:39]
	s_setprio 0
	s_setprio 1
	v_mfma_f32_16x16x32_bf16 v[28:31], v[176:179], v[192:195], v[28:31]
	v_mfma_f32_16x16x32_bf16 v[24:27], v[184:187], v[192:195], v[24:27]
	v_mfma_f32_16x16x32_bf16 v[16:19], v[184:187], v[200:203], v[16:19]
	v_mfma_f32_16x16x32_bf16 v[20:23], v[176:179], v[200:203], v[20:23]
	v_mfma_f32_16x16x32_bf16 v[12:15], v[176:179], v[208:211], v[12:15]
	v_mfma_f32_16x16x32_bf16 v[8:11], v[184:187], v[208:211], v[8:11]
	v_mfma_f32_16x16x32_bf16 v[0:3], v[184:187], v[216:219], v[0:3]
	v_mfma_f32_16x16x32_bf16 v[4:7], v[176:179], v[216:219], v[4:7]
	v_mfma_f32_16x16x32_bf16 v[28:31], v[180:183], v[196:199], v[28:31]
	v_mfma_f32_16x16x32_bf16 v[24:27], v[188:191], v[196:199], v[24:27]
	v_mfma_f32_16x16x32_bf16 v[16:19], v[188:191], v[204:207], v[16:19]
	v_mfma_f32_16x16x32_bf16 v[20:23], v[180:183], v[204:207], v[20:23]
	v_mfma_f32_16x16x32_bf16 v[12:15], v[180:183], v[212:215], v[12:15]
	v_mfma_f32_16x16x32_bf16 v[8:11], v[188:191], v[212:215], v[8:11]
	v_mfma_f32_16x16x32_bf16 v[0:3], v[188:191], v[220:223], v[0:3]
	v_mfma_f32_16x16x32_bf16 v[4:7], v[180:183], v[220:223], v[4:7]
	s_setprio 0
	s_barrier
	s_add_i32 s54, s54, 2
	s_add_u32 s24, s24, 0x100
	s_addc_u32 s25, s25, 0
	s_add_u32 s52, s52, 0x100
	s_addc_u32 s53, s53, 0
	s_cmp_gt_u32 s54, 61
	s_cbranch_scc0 .LBB0_687
	s_and_b64 vcc, exec, s[12:13]
	s_cbranch_vccz .LBB0_690
	s_barrier
